# rotate
# baseline (speedup 1.0000x reference)
.LBB3_23:
	s_andn2_b64 vcc, exec, s[24:25]
	s_cbranch_vccnz .LBB3_26
	s_mov_b32 s67, 0
	s_mov_b32 s8, 64
	s_waitcnt vmcnt(3)
	s_add_i32 s67, s67, 1
	v_and_or_b32 v74, v58, v105, s19
	v_and_or_b32 v75, v59, v105, s19
	v_and_or_b32 v76, v60, v105, s19
	v_and_or_b32 v77, v61, v105, s19
	s_lshl_b64 s[24:25], s[8:9], 4
	ds_read_b128 v[240:243], v74
	ds_read_b128 v[98:101], v75
	ds_read_b128 v[94:97], v76
	ds_read_b128 v[74:77], v77
	s_waitcnt vmcnt(2)
	s_add_u32 s26, s45, s24
	v_and_or_b32 v78, v62, v105, s19
	v_and_or_b32 v79, v63, v105, s19
	v_and_or_b32 v80, v64, v105, s19
	v_and_or_b32 v81, v65, v105, s19
	s_addc_u32 s27, s46, s25
	ds_read_b128 v[90:93], v78
	ds_read_b128 v[86:89], v79
	ds_read_b128 v[82:85], v80
	ds_read_b128 v[78:81], v81
.LBB3_25:
	s_waitcnt lgkmcnt(4)
	s_add_u32 s28, s47, s24
	v_fma_mix_f32 v182, v240, v58, v182 op_sel:[0,1,0] op_sel_hi:[1,1,0]
	v_fma_mix_f32 v183, v240, v58, v183 op_sel:[1,1,0] op_sel_hi:[1,1,0]
	v_fma_mix_f32 v184, v241, v58, v184 op_sel:[0,1,0] op_sel_hi:[1,1,0]
	v_fma_mix_f32 v185, v241, v58, v185 op_sel:[1,1,0] op_sel_hi:[1,1,0]
	v_fma_mix_f32 v186, v242, v58, v186 op_sel:[0,1,0] op_sel_hi:[1,1,0]
	v_fma_mix_f32 v187, v242, v58, v187 op_sel:[1,1,0] op_sel_hi:[1,1,0]
	v_fma_mix_f32 v188, v243, v58, v188 op_sel:[0,1,0] op_sel_hi:[1,1,0]
	v_fma_mix_f32 v189, v243, v58, v189 op_sel:[1,1,0] op_sel_hi:[1,1,0]
	v_fma_mix_f32 v182, v98, v59, v182 op_sel:[0,1,0] op_sel_hi:[1,1,0]
	v_fma_mix_f32 v183, v98, v59, v183 op_sel:[1,1,0] op_sel_hi:[1,1,0]
	v_fma_mix_f32 v184, v99, v59, v184 op_sel:[0,1,0] op_sel_hi:[1,1,0]
	v_fma_mix_f32 v185, v99, v59, v185 op_sel:[1,1,0] op_sel_hi:[1,1,0]
	v_fma_mix_f32 v186, v100, v59, v186 op_sel:[0,1,0] op_sel_hi:[1,1,0]
	v_fma_mix_f32 v187, v100, v59, v187 op_sel:[1,1,0] op_sel_hi:[1,1,0]
	v_fma_mix_f32 v188, v101, v59, v188 op_sel:[0,1,0] op_sel_hi:[1,1,0]
	v_fma_mix_f32 v189, v101, v59, v189 op_sel:[1,1,0] op_sel_hi:[1,1,0]
	v_fma_mix_f32 v182, v94, v60, v182 op_sel:[0,1,0] op_sel_hi:[1,1,0]
	v_fma_mix_f32 v183, v94, v60, v183 op_sel:[1,1,0] op_sel_hi:[1,1,0]
	v_fma_mix_f32 v184, v95, v60, v184 op_sel:[0,1,0] op_sel_hi:[1,1,0]
	v_fma_mix_f32 v185, v95, v60, v185 op_sel:[1,1,0] op_sel_hi:[1,1,0]
	v_fma_mix_f32 v186, v96, v60, v186 op_sel:[0,1,0] op_sel_hi:[1,1,0]
	v_fma_mix_f32 v187, v96, v60, v187 op_sel:[1,1,0] op_sel_hi:[1,1,0]
	v_fma_mix_f32 v188, v97, v60, v188 op_sel:[0,1,0] op_sel_hi:[1,1,0]
	v_fma_mix_f32 v189, v97, v60, v189 op_sel:[1,1,0] op_sel_hi:[1,1,0]
	v_fma_mix_f32 v182, v74, v61, v182 op_sel:[0,1,0] op_sel_hi:[1,1,0]
	v_fma_mix_f32 v183, v74, v61, v183 op_sel:[1,1,0] op_sel_hi:[1,1,0]
	v_fma_mix_f32 v184, v75, v61, v184 op_sel:[0,1,0] op_sel_hi:[1,1,0]
	v_fma_mix_f32 v185, v75, v61, v185 op_sel:[1,1,0] op_sel_hi:[1,1,0]
	v_fma_mix_f32 v186, v76, v61, v186 op_sel:[0,1,0] op_sel_hi:[1,1,0]
	v_fma_mix_f32 v187, v76, v61, v187 op_sel:[1,1,0] op_sel_hi:[1,1,0]
	v_fma_mix_f32 v188, v77, v61, v188 op_sel:[0,1,0] op_sel_hi:[1,1,0]
	v_fma_mix_f32 v189, v77, v61, v189 op_sel:[1,1,0] op_sel_hi:[1,1,0]
	global_load_dwordx4 v[58:61], v104, s[26:27]
	s_waitcnt vmcnt(2)
	s_addc_u32 s29, s48, s25
	v_and_or_b32 v74, v66, v105, s19
	v_and_or_b32 v94, v67, v105, s19
	v_and_or_b32 v98, v68, v105, s19
	v_and_or_b32 v240, v69, v105, s19
	s_add_u32 s30, s49, s24
	ds_read_b128 v[74:77], v74
	ds_read_b128 v[94:97], v94
	ds_read_b128 v[98:101], v98
	ds_read_b128 v[240:243], v240
	s_waitcnt lgkmcnt(4)
	s_addc_u32 s31, s50, s25
	v_fma_mix_f32 v198, v90, v62, v198 op_sel:[0,1,0] op_sel_hi:[1,1,0]
	v_fma_mix_f32 v199, v90, v62, v199 op_sel:[1,1,0] op_sel_hi:[1,1,0]
	v_fma_mix_f32 v200, v91, v62, v200 op_sel:[0,1,0] op_sel_hi:[1,1,0]
	v_fma_mix_f32 v201, v91, v62, v201 op_sel:[1,1,0] op_sel_hi:[1,1,0]
	v_fma_mix_f32 v202, v92, v62, v202 op_sel:[0,1,0] op_sel_hi:[1,1,0]
	v_fma_mix_f32 v203, v92, v62, v203 op_sel:[1,1,0] op_sel_hi:[1,1,0]
	v_fma_mix_f32 v204, v93, v62, v204 op_sel:[0,1,0] op_sel_hi:[1,1,0]
	v_fma_mix_f32 v205, v93, v62, v205 op_sel:[1,1,0] op_sel_hi:[1,1,0]
	v_fma_mix_f32 v198, v86, v63, v198 op_sel:[0,1,0] op_sel_hi:[1,1,0]
	v_fma_mix_f32 v199, v86, v63, v199 op_sel:[1,1,0] op_sel_hi:[1,1,0]
	v_fma_mix_f32 v200, v87, v63, v200 op_sel:[0,1,0] op_sel_hi:[1,1,0]
	v_fma_mix_f32 v201, v87, v63, v201 op_sel:[1,1,0] op_sel_hi:[1,1,0]
	v_fma_mix_f32 v202, v88, v63, v202 op_sel:[0,1,0] op_sel_hi:[1,1,0]
	v_fma_mix_f32 v203, v88, v63, v203 op_sel:[1,1,0] op_sel_hi:[1,1,0]
	v_fma_mix_f32 v204, v89, v63, v204 op_sel:[0,1,0] op_sel_hi:[1,1,0]
	v_fma_mix_f32 v205, v89, v63, v205 op_sel:[1,1,0] op_sel_hi:[1,1,0]
	v_fma_mix_f32 v198, v82, v64, v198 op_sel:[0,1,0] op_sel_hi:[1,1,0]
	v_fma_mix_f32 v199, v82, v64, v199 op_sel:[1,1,0] op_sel_hi:[1,1,0]
	v_fma_mix_f32 v200, v83, v64, v200 op_sel:[0,1,0] op_sel_hi:[1,1,0]
	v_fma_mix_f32 v201, v83, v64, v201 op_sel:[1,1,0] op_sel_hi:[1,1,0]
	v_fma_mix_f32 v202, v84, v64, v202 op_sel:[0,1,0] op_sel_hi:[1,1,0]
	v_fma_mix_f32 v203, v84, v64, v203 op_sel:[1,1,0] op_sel_hi:[1,1,0]
	v_fma_mix_f32 v204, v85, v64, v204 op_sel:[0,1,0] op_sel_hi:[1,1,0]
	v_fma_mix_f32 v205, v85, v64, v205 op_sel:[1,1,0] op_sel_hi:[1,1,0]
	v_fma_mix_f32 v198, v78, v65, v198 op_sel:[0,1,0] op_sel_hi:[1,1,0]
	v_fma_mix_f32 v199, v78, v65, v199 op_sel:[1,1,0] op_sel_hi:[1,1,0]
	v_fma_mix_f32 v200, v79, v65, v200 op_sel:[0,1,0] op_sel_hi:[1,1,0]
	v_fma_mix_f32 v201, v79, v65, v201 op_sel:[1,1,0] op_sel_hi:[1,1,0]
	v_fma_mix_f32 v202, v80, v65, v202 op_sel:[0,1,0] op_sel_hi:[1,1,0]
	v_fma_mix_f32 v203, v80, v65, v203 op_sel:[1,1,0] op_sel_hi:[1,1,0]
	v_fma_mix_f32 v204, v81, v65, v204 op_sel:[0,1,0] op_sel_hi:[1,1,0]
	v_fma_mix_f32 v205, v81, v65, v205 op_sel:[1,1,0] op_sel_hi:[1,1,0]
	global_load_dwordx4 v[62:65], v104, s[28:29]
	s_waitcnt vmcnt(2)
	s_add_u32 s24, s51, s24
	v_and_or_b32 v78, v70, v105, s19
	v_and_or_b32 v82, v71, v105, s19
	v_and_or_b32 v86, v72, v105, s19
	v_and_or_b32 v90, v73, v105, s19
	s_addc_u32 s25, s52, s25
	ds_read_b128 v[78:81], v78
	ds_read_b128 v[82:85], v82
	ds_read_b128 v[86:89], v86
	ds_read_b128 v[90:93], v90
	s_waitcnt lgkmcnt(4)
	s_add_i32 s8, s8, 64
	v_fma_mix_f32 v214, v74, v66, v214 op_sel:[0,1,0] op_sel_hi:[1,1,0]
	v_fma_mix_f32 v215, v74, v66, v215 op_sel:[1,1,0] op_sel_hi:[1,1,0]
	v_fma_mix_f32 v216, v75, v66, v216 op_sel:[0,1,0] op_sel_hi:[1,1,0]
	v_fma_mix_f32 v217, v75, v66, v217 op_sel:[1,1,0] op_sel_hi:[1,1,0]
	v_fma_mix_f32 v218, v76, v66, v218 op_sel:[0,1,0] op_sel_hi:[1,1,0]
	v_fma_mix_f32 v219, v76, v66, v219 op_sel:[1,1,0] op_sel_hi:[1,1,0]
	v_fma_mix_f32 v220, v77, v66, v220 op_sel:[0,1,0] op_sel_hi:[1,1,0]
	v_fma_mix_f32 v221, v77, v66, v221 op_sel:[1,1,0] op_sel_hi:[1,1,0]
	v_fma_mix_f32 v214, v94, v67, v214 op_sel:[0,1,0] op_sel_hi:[1,1,0]
	v_fma_mix_f32 v215, v94, v67, v215 op_sel:[1,1,0] op_sel_hi:[1,1,0]
	v_fma_mix_f32 v216, v95, v67, v216 op_sel:[0,1,0] op_sel_hi:[1,1,0]
	v_fma_mix_f32 v217, v95, v67, v217 op_sel:[1,1,0] op_sel_hi:[1,1,0]
	v_fma_mix_f32 v218, v96, v67, v218 op_sel:[0,1,0] op_sel_hi:[1,1,0]
	v_fma_mix_f32 v219, v96, v67, v219 op_sel:[1,1,0] op_sel_hi:[1,1,0]
	v_fma_mix_f32 v220, v97, v67, v220 op_sel:[0,1,0] op_sel_hi:[1,1,0]
	v_fma_mix_f32 v221, v97, v67, v221 op_sel:[1,1,0] op_sel_hi:[1,1,0]
	v_fma_mix_f32 v214, v98, v68, v214 op_sel:[0,1,0] op_sel_hi:[1,1,0]
	v_fma_mix_f32 v215, v98, v68, v215 op_sel:[1,1,0] op_sel_hi:[1,1,0]
	v_fma_mix_f32 v216, v99, v68, v216 op_sel:[0,1,0] op_sel_hi:[1,1,0]
	v_fma_mix_f32 v217, v99, v68, v217 op_sel:[1,1,0] op_sel_hi:[1,1,0]
	v_fma_mix_f32 v218, v100, v68, v218 op_sel:[0,1,0] op_sel_hi:[1,1,0]
	v_fma_mix_f32 v219, v100, v68, v219 op_sel:[1,1,0] op_sel_hi:[1,1,0]
	v_fma_mix_f32 v220, v101, v68, v220 op_sel:[0,1,0] op_sel_hi:[1,1,0]
	v_fma_mix_f32 v221, v101, v68, v221 op_sel:[1,1,0] op_sel_hi:[1,1,0]
	v_fma_mix_f32 v214, v240, v69, v214 op_sel:[0,1,0] op_sel_hi:[1,1,0]
	v_fma_mix_f32 v215, v240, v69, v215 op_sel:[1,1,0] op_sel_hi:[1,1,0]
	v_fma_mix_f32 v216, v241, v69, v216 op_sel:[0,1,0] op_sel_hi:[1,1,0]
	v_fma_mix_f32 v217, v241, v69, v217 op_sel:[1,1,0] op_sel_hi:[1,1,0]
	v_fma_mix_f32 v218, v242, v69, v218 op_sel:[0,1,0] op_sel_hi:[1,1,0]
	v_fma_mix_f32 v219, v242, v69, v219 op_sel:[1,1,0] op_sel_hi:[1,1,0]
	v_fma_mix_f32 v220, v243, v69, v220 op_sel:[0,1,0] op_sel_hi:[1,1,0]
	v_fma_mix_f32 v221, v243, v69, v221 op_sel:[1,1,0] op_sel_hi:[1,1,0]
	global_load_dwordx4 v[66:69], v104, s[30:31]
	s_waitcnt vmcnt(2)
	v_and_or_b32 v74, v58, v105, s19
	v_and_or_b32 v75, v59, v105, s19
	v_and_or_b32 v76, v60, v105, s19
	v_and_or_b32 v77, v61, v105, s19
	ds_read_b128 v[240:243], v74
	ds_read_b128 v[98:101], v75
	ds_read_b128 v[94:97], v76
	ds_read_b128 v[74:77], v77
	s_waitcnt lgkmcnt(4)
	v_fma_mix_f32 v222, v78, v70, v222 op_sel:[0,1,0] op_sel_hi:[1,1,0]
	v_fma_mix_f32 v223, v78, v70, v223 op_sel:[1,1,0] op_sel_hi:[1,1,0]
	v_fma_mix_f32 v224, v79, v70, v224 op_sel:[0,1,0] op_sel_hi:[1,1,0]
	v_fma_mix_f32 v225, v79, v70, v225 op_sel:[1,1,0] op_sel_hi:[1,1,0]
	v_fma_mix_f32 v226, v80, v70, v226 op_sel:[0,1,0] op_sel_hi:[1,1,0]
	v_fma_mix_f32 v227, v80, v70, v227 op_sel:[1,1,0] op_sel_hi:[1,1,0]
	v_fma_mix_f32 v228, v81, v70, v228 op_sel:[0,1,0] op_sel_hi:[1,1,0]
	v_fma_mix_f32 v229, v81, v70, v229 op_sel:[1,1,0] op_sel_hi:[1,1,0]
	v_fma_mix_f32 v222, v82, v71, v222 op_sel:[0,1,0] op_sel_hi:[1,1,0]
	v_fma_mix_f32 v223, v82, v71, v223 op_sel:[1,1,0] op_sel_hi:[1,1,0]
	v_fma_mix_f32 v224, v83, v71, v224 op_sel:[0,1,0] op_sel_hi:[1,1,0]
	v_fma_mix_f32 v225, v83, v71, v225 op_sel:[1,1,0] op_sel_hi:[1,1,0]
	v_fma_mix_f32 v226, v84, v71, v226 op_sel:[0,1,0] op_sel_hi:[1,1,0]
	v_fma_mix_f32 v227, v84, v71, v227 op_sel:[1,1,0] op_sel_hi:[1,1,0]
	v_fma_mix_f32 v228, v85, v71, v228 op_sel:[0,1,0] op_sel_hi:[1,1,0]
	v_fma_mix_f32 v229, v85, v71, v229 op_sel:[1,1,0] op_sel_hi:[1,1,0]
	v_fma_mix_f32 v222, v86, v72, v222 op_sel:[0,1,0] op_sel_hi:[1,1,0]
	v_fma_mix_f32 v223, v86, v72, v223 op_sel:[1,1,0] op_sel_hi:[1,1,0]
	v_fma_mix_f32 v224, v87, v72, v224 op_sel:[0,1,0] op_sel_hi:[1,1,0]
	v_fma_mix_f32 v225, v87, v72, v225 op_sel:[1,1,0] op_sel_hi:[1,1,0]
	v_fma_mix_f32 v226, v88, v72, v226 op_sel:[0,1,0] op_sel_hi:[1,1,0]
	v_fma_mix_f32 v227, v88, v72, v227 op_sel:[1,1,0] op_sel_hi:[1,1,0]
	v_fma_mix_f32 v228, v89, v72, v228 op_sel:[0,1,0] op_sel_hi:[1,1,0]
	v_fma_mix_f32 v229, v89, v72, v229 op_sel:[1,1,0] op_sel_hi:[1,1,0]
	v_fma_mix_f32 v222, v90, v73, v222 op_sel:[0,1,0] op_sel_hi:[1,1,0]
	v_fma_mix_f32 v223, v90, v73, v223 op_sel:[1,1,0] op_sel_hi:[1,1,0]
	v_fma_mix_f32 v224, v91, v73, v224 op_sel:[0,1,0] op_sel_hi:[1,1,0]
	v_fma_mix_f32 v225, v91, v73, v225 op_sel:[1,1,0] op_sel_hi:[1,1,0]
	v_fma_mix_f32 v226, v92, v73, v226 op_sel:[0,1,0] op_sel_hi:[1,1,0]
	v_fma_mix_f32 v227, v92, v73, v227 op_sel:[1,1,0] op_sel_hi:[1,1,0]
	v_fma_mix_f32 v228, v93, v73, v228 op_sel:[0,1,0] op_sel_hi:[1,1,0]
	v_fma_mix_f32 v229, v93, v73, v229 op_sel:[1,1,0] op_sel_hi:[1,1,0]
	global_load_dwordx4 v[70:73], v104, s[24:25]
	s_add_i32 s67, s67, 1
	s_lshl_b64 s[24:25], s[8:9], 4
	s_waitcnt vmcnt(2)
	s_add_u32 s26, s45, s24
	v_and_or_b32 v78, v62, v105, s19
	v_and_or_b32 v79, v63, v105, s19
	v_and_or_b32 v80, v64, v105, s19
	v_and_or_b32 v81, v65, v105, s19
	s_addc_u32 s27, s46, s25
	ds_read_b128 v[90:93], v78
	ds_read_b128 v[86:89], v79
	ds_read_b128 v[82:85], v80
	ds_read_b128 v[78:81], v81
	s_cmp_gt_i32 s67, s36
	s_cbranch_scc0 .LBB3_25
	s_waitcnt lgkmcnt(0)

.LBB3_38:
	s_andn2_b64 vcc, exec, s[24:25]
	s_cbranch_vccnz .LBB3_41
	s_mov_b32 s68, 0
	s_mov_b32 s8, 64
	s_waitcnt vmcnt(3)
	s_add_i32 s68, s68, 1
	v_and_or_b32 v74, v58, v105, s19
	v_and_or_b32 v75, v59, v105, s19
	v_and_or_b32 v76, v60, v105, s19
	v_and_or_b32 v77, v61, v105, s19
	s_lshl_b64 s[24:25], s[8:9], 4
	ds_read_b128 v[242:245], v74
	ds_read_b128 v[98:101], v75
	ds_read_b128 v[94:97], v76
	ds_read_b128 v[74:77], v77
	s_waitcnt vmcnt(2)
	s_add_u32 s26, s53, s24
	v_and_or_b32 v78, v62, v105, s19
	v_and_or_b32 v79, v63, v105, s19
	v_and_or_b32 v80, v64, v105, s19
	v_and_or_b32 v81, v65, v105, s19
	s_addc_u32 s27, s54, s25
	ds_read_b128 v[90:93], v78
	ds_read_b128 v[86:89], v79
	ds_read_b128 v[82:85], v80
	ds_read_b128 v[78:81], v81
.LBB3_40:
	s_waitcnt lgkmcnt(4)
	s_add_u32 s28, s55, s24
	v_fma_mix_f32 v206, v242, v58, v206 op_sel:[0,1,0] op_sel_hi:[1,1,0]
	v_fma_mix_f32 v207, v242, v58, v207 op_sel:[1,1,0] op_sel_hi:[1,1,0]
	v_fma_mix_f32 v208, v243, v58, v208 op_sel:[0,1,0] op_sel_hi:[1,1,0]
	v_fma_mix_f32 v209, v243, v58, v209 op_sel:[1,1,0] op_sel_hi:[1,1,0]
	v_fma_mix_f32 v210, v244, v58, v210 op_sel:[0,1,0] op_sel_hi:[1,1,0]
	v_fma_mix_f32 v211, v244, v58, v211 op_sel:[1,1,0] op_sel_hi:[1,1,0]
	v_fma_mix_f32 v212, v245, v58, v212 op_sel:[0,1,0] op_sel_hi:[1,1,0]
	v_fma_mix_f32 v213, v245, v58, v213 op_sel:[1,1,0] op_sel_hi:[1,1,0]
	v_fma_mix_f32 v206, v98, v59, v206 op_sel:[0,1,0] op_sel_hi:[1,1,0]
	v_fma_mix_f32 v207, v98, v59, v207 op_sel:[1,1,0] op_sel_hi:[1,1,0]
	v_fma_mix_f32 v208, v99, v59, v208 op_sel:[0,1,0] op_sel_hi:[1,1,0]
	v_fma_mix_f32 v209, v99, v59, v209 op_sel:[1,1,0] op_sel_hi:[1,1,0]
	v_fma_mix_f32 v210, v100, v59, v210 op_sel:[0,1,0] op_sel_hi:[1,1,0]
	v_fma_mix_f32 v211, v100, v59, v211 op_sel:[1,1,0] op_sel_hi:[1,1,0]
	v_fma_mix_f32 v212, v101, v59, v212 op_sel:[0,1,0] op_sel_hi:[1,1,0]
	v_fma_mix_f32 v213, v101, v59, v213 op_sel:[1,1,0] op_sel_hi:[1,1,0]
	v_fma_mix_f32 v206, v94, v60, v206 op_sel:[0,1,0] op_sel_hi:[1,1,0]
	v_fma_mix_f32 v207, v94, v60, v207 op_sel:[1,1,0] op_sel_hi:[1,1,0]
	v_fma_mix_f32 v208, v95, v60, v208 op_sel:[0,1,0] op_sel_hi:[1,1,0]
	v_fma_mix_f32 v209, v95, v60, v209 op_sel:[1,1,0] op_sel_hi:[1,1,0]
	v_fma_mix_f32 v210, v96, v60, v210 op_sel:[0,1,0] op_sel_hi:[1,1,0]
	v_fma_mix_f32 v211, v96, v60, v211 op_sel:[1,1,0] op_sel_hi:[1,1,0]
	v_fma_mix_f32 v212, v97, v60, v212 op_sel:[0,1,0] op_sel_hi:[1,1,0]
	v_fma_mix_f32 v213, v97, v60, v213 op_sel:[1,1,0] op_sel_hi:[1,1,0]
	v_fma_mix_f32 v206, v74, v61, v206 op_sel:[0,1,0] op_sel_hi:[1,1,0]
	v_fma_mix_f32 v207, v74, v61, v207 op_sel:[1,1,0] op_sel_hi:[1,1,0]
	v_fma_mix_f32 v208, v75, v61, v208 op_sel:[0,1,0] op_sel_hi:[1,1,0]
	v_fma_mix_f32 v209, v75, v61, v209 op_sel:[1,1,0] op_sel_hi:[1,1,0]
	v_fma_mix_f32 v210, v76, v61, v210 op_sel:[0,1,0] op_sel_hi:[1,1,0]
	v_fma_mix_f32 v211, v76, v61, v211 op_sel:[1,1,0] op_sel_hi:[1,1,0]
	v_fma_mix_f32 v212, v77, v61, v212 op_sel:[0,1,0] op_sel_hi:[1,1,0]
	v_fma_mix_f32 v213, v77, v61, v213 op_sel:[1,1,0] op_sel_hi:[1,1,0]
	global_load_dwordx4 v[58:61], v104, s[26:27]
	s_waitcnt vmcnt(2)
	s_addc_u32 s29, s56, s25
	v_and_or_b32 v74, v66, v105, s19
	v_and_or_b32 v94, v67, v105, s19
	v_and_or_b32 v98, v68, v105, s19
	v_and_or_b32 v231, v69, v105, s19
	s_add_u32 s30, s57, s24
	ds_read_b128 v[74:77], v74
	ds_read_b128 v[94:97], v94
	ds_read_b128 v[98:101], v98
	ds_read_b128 v[242:245], v231
	s_waitcnt lgkmcnt(4)
	s_addc_u32 s31, s58, s25
	v_fma_mix_f32 v190, v90, v62, v190 op_sel:[0,1,0] op_sel_hi:[1,1,0]
	v_fma_mix_f32 v191, v90, v62, v191 op_sel:[1,1,0] op_sel_hi:[1,1,0]
	v_fma_mix_f32 v192, v91, v62, v192 op_sel:[0,1,0] op_sel_hi:[1,1,0]
	v_fma_mix_f32 v193, v91, v62, v193 op_sel:[1,1,0] op_sel_hi:[1,1,0]
	v_fma_mix_f32 v194, v92, v62, v194 op_sel:[0,1,0] op_sel_hi:[1,1,0]
	v_fma_mix_f32 v195, v92, v62, v195 op_sel:[1,1,0] op_sel_hi:[1,1,0]
	v_fma_mix_f32 v196, v93, v62, v196 op_sel:[0,1,0] op_sel_hi:[1,1,0]
	v_fma_mix_f32 v197, v93, v62, v197 op_sel:[1,1,0] op_sel_hi:[1,1,0]
	v_fma_mix_f32 v190, v86, v63, v190 op_sel:[0,1,0] op_sel_hi:[1,1,0]
	v_fma_mix_f32 v191, v86, v63, v191 op_sel:[1,1,0] op_sel_hi:[1,1,0]
	v_fma_mix_f32 v192, v87, v63, v192 op_sel:[0,1,0] op_sel_hi:[1,1,0]
	v_fma_mix_f32 v193, v87, v63, v193 op_sel:[1,1,0] op_sel_hi:[1,1,0]
	v_fma_mix_f32 v194, v88, v63, v194 op_sel:[0,1,0] op_sel_hi:[1,1,0]
	v_fma_mix_f32 v195, v88, v63, v195 op_sel:[1,1,0] op_sel_hi:[1,1,0]
	v_fma_mix_f32 v196, v89, v63, v196 op_sel:[0,1,0] op_sel_hi:[1,1,0]
	v_fma_mix_f32 v197, v89, v63, v197 op_sel:[1,1,0] op_sel_hi:[1,1,0]
	v_fma_mix_f32 v190, v82, v64, v190 op_sel:[0,1,0] op_sel_hi:[1,1,0]
	v_fma_mix_f32 v191, v82, v64, v191 op_sel:[1,1,0] op_sel_hi:[1,1,0]
	v_fma_mix_f32 v192, v83, v64, v192 op_sel:[0,1,0] op_sel_hi:[1,1,0]
	v_fma_mix_f32 v193, v83, v64, v193 op_sel:[1,1,0] op_sel_hi:[1,1,0]
	v_fma_mix_f32 v194, v84, v64, v194 op_sel:[0,1,0] op_sel_hi:[1,1,0]
	v_fma_mix_f32 v195, v84, v64, v195 op_sel:[1,1,0] op_sel_hi:[1,1,0]
	v_fma_mix_f32 v196, v85, v64, v196 op_sel:[0,1,0] op_sel_hi:[1,1,0]
	v_fma_mix_f32 v197, v85, v64, v197 op_sel:[1,1,0] op_sel_hi:[1,1,0]
	v_fma_mix_f32 v190, v78, v65, v190 op_sel:[0,1,0] op_sel_hi:[1,1,0]
	v_fma_mix_f32 v191, v78, v65, v191 op_sel:[1,1,0] op_sel_hi:[1,1,0]
	v_fma_mix_f32 v192, v79, v65, v192 op_sel:[0,1,0] op_sel_hi:[1,1,0]
	v_fma_mix_f32 v193, v79, v65, v193 op_sel:[1,1,0] op_sel_hi:[1,1,0]
	v_fma_mix_f32 v194, v80, v65, v194 op_sel:[0,1,0] op_sel_hi:[1,1,0]
	v_fma_mix_f32 v195, v80, v65, v195 op_sel:[1,1,0] op_sel_hi:[1,1,0]
	v_fma_mix_f32 v196, v81, v65, v196 op_sel:[0,1,0] op_sel_hi:[1,1,0]
	v_fma_mix_f32 v197, v81, v65, v197 op_sel:[1,1,0] op_sel_hi:[1,1,0]
	global_load_dwordx4 v[62:65], v104, s[28:29]
	s_waitcnt vmcnt(2)
	s_add_u32 s24, s59, s24
	v_and_or_b32 v78, v70, v105, s19
	v_and_or_b32 v82, v71, v105, s19
	v_and_or_b32 v86, v72, v105, s19
	v_and_or_b32 v90, v73, v105, s19
	s_addc_u32 s25, s60, s25
	ds_read_b128 v[78:81], v78
	ds_read_b128 v[82:85], v82
	ds_read_b128 v[86:89], v86
	ds_read_b128 v[90:93], v90
	s_waitcnt lgkmcnt(4)
	s_add_i32 s8, s8, 64
	v_fma_mix_f32 v174, v74, v66, v174 op_sel:[0,1,0] op_sel_hi:[1,1,0]
	v_fma_mix_f32 v175, v74, v66, v175 op_sel:[1,1,0] op_sel_hi:[1,1,0]
	v_fma_mix_f32 v176, v75, v66, v176 op_sel:[0,1,0] op_sel_hi:[1,1,0]
	v_fma_mix_f32 v177, v75, v66, v177 op_sel:[1,1,0] op_sel_hi:[1,1,0]
	v_fma_mix_f32 v178, v76, v66, v178 op_sel:[0,1,0] op_sel_hi:[1,1,0]
	v_fma_mix_f32 v179, v76, v66, v179 op_sel:[1,1,0] op_sel_hi:[1,1,0]
	v_fma_mix_f32 v180, v77, v66, v180 op_sel:[0,1,0] op_sel_hi:[1,1,0]
	v_fma_mix_f32 v181, v77, v66, v181 op_sel:[1,1,0] op_sel_hi:[1,1,0]
	v_fma_mix_f32 v174, v94, v67, v174 op_sel:[0,1,0] op_sel_hi:[1,1,0]
	v_fma_mix_f32 v175, v94, v67, v175 op_sel:[1,1,0] op_sel_hi:[1,1,0]
	v_fma_mix_f32 v176, v95, v67, v176 op_sel:[0,1,0] op_sel_hi:[1,1,0]
	v_fma_mix_f32 v177, v95, v67, v177 op_sel:[1,1,0] op_sel_hi:[1,1,0]
	v_fma_mix_f32 v178, v96, v67, v178 op_sel:[0,1,0] op_sel_hi:[1,1,0]
	v_fma_mix_f32 v179, v96, v67, v179 op_sel:[1,1,0] op_sel_hi:[1,1,0]
	v_fma_mix_f32 v180, v97, v67, v180 op_sel:[0,1,0] op_sel_hi:[1,1,0]
	v_fma_mix_f32 v181, v97, v67, v181 op_sel:[1,1,0] op_sel_hi:[1,1,0]
	v_fma_mix_f32 v174, v98, v68, v174 op_sel:[0,1,0] op_sel_hi:[1,1,0]
	v_fma_mix_f32 v175, v98, v68, v175 op_sel:[1,1,0] op_sel_hi:[1,1,0]
	v_fma_mix_f32 v176, v99, v68, v176 op_sel:[0,1,0] op_sel_hi:[1,1,0]
	v_fma_mix_f32 v177, v99, v68, v177 op_sel:[1,1,0] op_sel_hi:[1,1,0]
	v_fma_mix_f32 v178, v100, v68, v178 op_sel:[0,1,0] op_sel_hi:[1,1,0]
	v_fma_mix_f32 v179, v100, v68, v179 op_sel:[1,1,0] op_sel_hi:[1,1,0]
	v_fma_mix_f32 v180, v101, v68, v180 op_sel:[0,1,0] op_sel_hi:[1,1,0]
	v_fma_mix_f32 v181, v101, v68, v181 op_sel:[1,1,0] op_sel_hi:[1,1,0]
	v_fma_mix_f32 v174, v242, v69, v174 op_sel:[0,1,0] op_sel_hi:[1,1,0]
	v_fma_mix_f32 v175, v242, v69, v175 op_sel:[1,1,0] op_sel_hi:[1,1,0]
	v_fma_mix_f32 v176, v243, v69, v176 op_sel:[0,1,0] op_sel_hi:[1,1,0]
	v_fma_mix_f32 v177, v243, v69, v177 op_sel:[1,1,0] op_sel_hi:[1,1,0]
	v_fma_mix_f32 v178, v244, v69, v178 op_sel:[0,1,0] op_sel_hi:[1,1,0]
	v_fma_mix_f32 v179, v244, v69, v179 op_sel:[1,1,0] op_sel_hi:[1,1,0]
	v_fma_mix_f32 v180, v245, v69, v180 op_sel:[0,1,0] op_sel_hi:[1,1,0]
	v_fma_mix_f32 v181, v245, v69, v181 op_sel:[1,1,0] op_sel_hi:[1,1,0]
	global_load_dwordx4 v[66:69], v104, s[30:31]
	s_waitcnt vmcnt(2)
	v_and_or_b32 v74, v58, v105, s19
	v_and_or_b32 v75, v59, v105, s19
	v_and_or_b32 v76, v60, v105, s19
	v_and_or_b32 v77, v61, v105, s19
	ds_read_b128 v[242:245], v74
	ds_read_b128 v[98:101], v75
	ds_read_b128 v[94:97], v76
	ds_read_b128 v[74:77], v77
	s_waitcnt lgkmcnt(4)
	v_fma_mix_f32 v166, v78, v70, v166 op_sel:[0,1,0] op_sel_hi:[1,1,0]
	v_fma_mix_f32 v167, v78, v70, v167 op_sel:[1,1,0] op_sel_hi:[1,1,0]
	v_fma_mix_f32 v168, v79, v70, v168 op_sel:[0,1,0] op_sel_hi:[1,1,0]
	v_fma_mix_f32 v169, v79, v70, v169 op_sel:[1,1,0] op_sel_hi:[1,1,0]
	v_fma_mix_f32 v170, v80, v70, v170 op_sel:[0,1,0] op_sel_hi:[1,1,0]
	v_fma_mix_f32 v171, v80, v70, v171 op_sel:[1,1,0] op_sel_hi:[1,1,0]
	v_fma_mix_f32 v172, v81, v70, v172 op_sel:[0,1,0] op_sel_hi:[1,1,0]
	v_fma_mix_f32 v173, v81, v70, v173 op_sel:[1,1,0] op_sel_hi:[1,1,0]
	v_fma_mix_f32 v166, v82, v71, v166 op_sel:[0,1,0] op_sel_hi:[1,1,0]
	v_fma_mix_f32 v167, v82, v71, v167 op_sel:[1,1,0] op_sel_hi:[1,1,0]
	v_fma_mix_f32 v168, v83, v71, v168 op_sel:[0,1,0] op_sel_hi:[1,1,0]
	v_fma_mix_f32 v169, v83, v71, v169 op_sel:[1,1,0] op_sel_hi:[1,1,0]
	v_fma_mix_f32 v170, v84, v71, v170 op_sel:[0,1,0] op_sel_hi:[1,1,0]
	v_fma_mix_f32 v171, v84, v71, v171 op_sel:[1,1,0] op_sel_hi:[1,1,0]
	v_fma_mix_f32 v172, v85, v71, v172 op_sel:[0,1,0] op_sel_hi:[1,1,0]
	v_fma_mix_f32 v173, v85, v71, v173 op_sel:[1,1,0] op_sel_hi:[1,1,0]
	v_fma_mix_f32 v166, v86, v72, v166 op_sel:[0,1,0] op_sel_hi:[1,1,0]
	v_fma_mix_f32 v167, v86, v72, v167 op_sel:[1,1,0] op_sel_hi:[1,1,0]
	v_fma_mix_f32 v168, v87, v72, v168 op_sel:[0,1,0] op_sel_hi:[1,1,0]
	v_fma_mix_f32 v169, v87, v72, v169 op_sel:[1,1,0] op_sel_hi:[1,1,0]
	v_fma_mix_f32 v170, v88, v72, v170 op_sel:[0,1,0] op_sel_hi:[1,1,0]
	v_fma_mix_f32 v171, v88, v72, v171 op_sel:[1,1,0] op_sel_hi:[1,1,0]
	v_fma_mix_f32 v172, v89, v72, v172 op_sel:[0,1,0] op_sel_hi:[1,1,0]
	v_fma_mix_f32 v173, v89, v72, v173 op_sel:[1,1,0] op_sel_hi:[1,1,0]
	v_fma_mix_f32 v166, v90, v73, v166 op_sel:[0,1,0] op_sel_hi:[1,1,0]
	v_fma_mix_f32 v167, v90, v73, v167 op_sel:[1,1,0] op_sel_hi:[1,1,0]
	v_fma_mix_f32 v168, v91, v73, v168 op_sel:[0,1,0] op_sel_hi:[1,1,0]
	v_fma_mix_f32 v169, v91, v73, v169 op_sel:[1,1,0] op_sel_hi:[1,1,0]
	v_fma_mix_f32 v170, v92, v73, v170 op_sel:[0,1,0] op_sel_hi:[1,1,0]
	v_fma_mix_f32 v171, v92, v73, v171 op_sel:[1,1,0] op_sel_hi:[1,1,0]
	v_fma_mix_f32 v172, v93, v73, v172 op_sel:[0,1,0] op_sel_hi:[1,1,0]
	v_fma_mix_f32 v173, v93, v73, v173 op_sel:[1,1,0] op_sel_hi:[1,1,0]
	global_load_dwordx4 v[70:73], v104, s[24:25]
	s_add_i32 s68, s68, 1
	s_lshl_b64 s[24:25], s[8:9], 4
	s_waitcnt vmcnt(2)
	s_add_u32 s26, s53, s24
	v_and_or_b32 v78, v62, v105, s19
	v_and_or_b32 v79, v63, v105, s19
	v_and_or_b32 v80, v64, v105, s19
	v_and_or_b32 v81, v65, v105, s19
	s_addc_u32 s27, s54, s25
	ds_read_b128 v[90:93], v78
	ds_read_b128 v[86:89], v79
	ds_read_b128 v[82:85], v80
	ds_read_b128 v[78:81], v81
	s_cmp_le_i32 s68, s40
	s_cbranch_scc1 .LBB3_40
	s_waitcnt lgkmcnt(0)
